# topic loop rewritten: weights pre-halved, linear term folded into chain init, tc fragments double-buffered from LDS
# speedup vs baseline: 1.0377x; 1.0027x over previous
.LBB1_53:
	s_or_b64 exec, exec, s[2:3]
	v_add_f32_e32 v130, v130, v14
	v_or_b32_e32 v14, v212, v214
	v_add_f32_e32 v134, v134, v10
	v_add_f32_e32 v10, v110, v50
	v_add_f32_e32 v50, v98, v58
	v_add_f32_e32 v58, v90, v62
	v_add_u32_e32 v62, 0x17080, v14
	v_add_f32_e32 v131, v131, v15
	v_add_f32_e32 v132, v132, v16
	v_add_f32_e32 v133, v133, v17
	v_add_f32_e32 v82, v82, v30
	ds_read_b128 v[14:17], v62
	v_add_f32_e32 v83, v83, v31
	v_add_f32_e32 v84, v84, v32
	v_add_f32_e32 v85, v85, v33
	ds_read_b128 v[30:33], v62 offset:32
	v_add_f32_e32 v2, v142, v2
	v_add_f32_e32 v138, v138, v6
	v_add_f32_e32 v6, v126, v34
	v_add_f32_e32 v34, v122, v38
	v_add_f32_e32 v38, v118, v42
	v_add_f32_e32 v114, v114, v46
	v_add_f32_e32 v42, v106, v54
	v_add_f32_e32 v18, v102, v18
	v_add_f32_e32 v46, v94, v22
	v_add_f32_e32 v141, v141, v9
	v_add_f32_e32 v135, v135, v11
	v_add_f32_e32 v136, v136, v12
	v_add_f32_e32 v137, v137, v13
	v_add_f32_e32 v9, v129, v37
	v_add_f32_e32 v37, v125, v41
	v_add_f32_e32 v41, v121, v45
	v_add_f32_e32 v115, v115, v47
	v_add_f32_e32 v116, v116, v48
	v_add_f32_e32 v117, v117, v49
	v_add_f32_e32 v11, v111, v51
	v_add_f32_e32 v12, v112, v52
	v_add_f32_e32 v13, v113, v53
	v_add_f32_e32 v45, v109, v57
	v_add_f32_e32 v51, v99, v59
	v_add_f32_e32 v52, v100, v60
	v_add_f32_e32 v53, v101, v61
	v_add_f32_e32 v59, v91, v63
	v_add_f32_e32 v60, v92, v64
	v_add_f32_e32 v61, v93, v65
	v_add_f32_e32 v57, v86, v26
	s_waitcnt lgkmcnt(1)
	v_add_f32_e32 v2, v14, v2
	v_add_f32_e32 v6, v14, v6
	v_add_f32_e32 v10, v14, v10
	v_add_f32_e32 v14, v14, v18
	s_waitcnt lgkmcnt(0)
	v_add_f32_e32 v18, v30, v138
	v_add_f32_e32 v22, v30, v34
	v_add_f32_e32 v26, v30, v42
	v_add_f32_e32 v30, v30, v46
	ds_read_b128 v[46:49], v62 offset:64
	ds_read_b128 v[62:65], v62 offset:96
	v_add_f32_e32 v3, v143, v3
	v_add_f32_e32 v4, v144, v4
	v_add_f32_e32 v5, v145, v5
	v_add_f32_e32 v139, v139, v7
	v_add_f32_e32 v140, v140, v8
	v_add_f32_e32 v7, v127, v35
	v_add_f32_e32 v8, v128, v36
	v_add_f32_e32 v35, v123, v39
	v_add_f32_e32 v36, v124, v40
	v_add_f32_e32 v39, v119, v43
	v_add_f32_e32 v40, v120, v44
	v_add_f32_e32 v43, v107, v55
	v_add_f32_e32 v44, v108, v56
	v_add_f32_e32 v19, v103, v19
	v_add_f32_e32 v20, v104, v20
	v_add_f32_e32 v21, v105, v21
	v_add_f32_e32 v54, v95, v23
	v_add_f32_e32 v55, v96, v24
	v_add_f32_e32 v56, v97, v25
	v_add_f32_e32 v86, v87, v27
	v_add_f32_e32 v87, v88, v28
	v_add_f32_e32 v88, v89, v29
	v_add_f32_e32 v3, v15, v3
	v_add_f32_e32 v4, v16, v4
	v_add_f32_e32 v5, v17, v5
	v_add_f32_e32 v7, v15, v7
	v_add_f32_e32 v8, v16, v8
	v_add_f32_e32 v9, v17, v9
	v_add_f32_e32 v11, v15, v11
	v_add_f32_e32 v12, v16, v12
	v_add_f32_e32 v13, v17, v13
	v_add_f32_e32 v15, v15, v19
	v_add_f32_e32 v16, v16, v20
	v_add_f32_e32 v17, v17, v21
	v_add_f32_e32 v19, v31, v139
	v_add_f32_e32 v20, v32, v140
	v_add_f32_e32 v21, v33, v141
	v_add_f32_e32 v23, v31, v35
	v_add_f32_e32 v24, v32, v36
	v_add_f32_e32 v25, v33, v37
	v_add_f32_e32 v27, v31, v43
	v_add_f32_e32 v28, v32, v44
	v_add_f32_e32 v29, v33, v45
	v_add_f32_e32 v31, v31, v54
	v_add_f32_e32 v32, v32, v55
	v_add_f32_e32 v33, v33, v56
	s_waitcnt lgkmcnt(1)
	v_add_f32_e32 v34, v46, v134
	v_add_f32_e32 v38, v46, v38
	v_add_f32_e32 v42, v46, v50
	v_add_f32_e32 v43, v47, v51
	v_add_f32_e32 v44, v48, v52
	v_add_f32_e32 v45, v49, v53
	v_add_f32_e32 v46, v46, v57
	s_waitcnt lgkmcnt(0)
	v_add_f32_e32 v50, v62, v130
	v_add_f32_e32 v51, v63, v131
	v_add_f32_e32 v52, v64, v132
	v_add_f32_e32 v53, v65, v133
	v_add_f32_e32 v54, v62, v114
	v_add_f32_e32 v55, v63, v115
	v_add_f32_e32 v56, v64, v116
	v_add_f32_e32 v57, v65, v117
	v_add_f32_e32 v58, v62, v58
	v_add_f32_e32 v59, v63, v59
	v_add_f32_e32 v60, v64, v60
	v_add_f32_e32 v61, v65, v61
	v_add_f32_e32 v62, v62, v82
	v_add_f32_e32 v63, v63, v83
	v_add_f32_e32 v64, v64, v84
	v_add_f32_e32 v65, v65, v85
	s_waitcnt vmcnt(3)
	v_fma_f32 v82, v66, v2, 0
	v_fma_f32 v83, v66, v6, 0
	v_fma_f32 v84, v66, v10, 0
	v_fma_f32 v85, v66, v14, 0
	v_fmac_f32_e32 v82, v67, v3
	v_fmac_f32_e32 v83, v67, v7
	v_fmac_f32_e32 v84, v67, v11
	v_fmac_f32_e32 v85, v67, v15
	v_fmac_f32_e32 v82, v68, v4
	v_fmac_f32_e32 v83, v68, v8
	v_fmac_f32_e32 v84, v68, v12
	v_fmac_f32_e32 v85, v68, v16
	v_fmac_f32_e32 v82, v69, v5
	v_fmac_f32_e32 v83, v69, v9
	v_fmac_f32_e32 v84, v69, v13
	v_fmac_f32_e32 v85, v69, v17
	s_waitcnt vmcnt(2)
	v_fmac_f32_e32 v82, v70, v18
	v_fmac_f32_e32 v83, v70, v22
	v_fmac_f32_e32 v84, v70, v26
	v_fmac_f32_e32 v85, v70, v30
	v_fmac_f32_e32 v82, v71, v19
	v_fmac_f32_e32 v83, v71, v23
	v_fmac_f32_e32 v84, v71, v27
	v_fmac_f32_e32 v85, v71, v31
	v_fmac_f32_e32 v82, v72, v20
	v_fmac_f32_e32 v83, v72, v24
	v_fmac_f32_e32 v84, v72, v28
	v_fmac_f32_e32 v85, v72, v32
	v_fmac_f32_e32 v82, v73, v21
	v_fmac_f32_e32 v83, v73, v25
	v_fmac_f32_e32 v84, v73, v29
	v_fmac_f32_e32 v85, v73, v33
	v_add_f32_e32 v35, v47, v135
	v_add_f32_e32 v39, v47, v39
	v_add_f32_e32 v47, v47, v86
	s_waitcnt vmcnt(1)
	v_fmac_f32_e32 v82, v74, v34
	v_fmac_f32_e32 v83, v74, v38
	v_fmac_f32_e32 v84, v74, v42
	v_fmac_f32_e32 v85, v74, v46
	v_add_f32_e32 v36, v48, v136
	v_add_f32_e32 v40, v48, v40
	v_add_f32_e32 v48, v48, v87
	v_fmac_f32_e32 v82, v75, v35
	v_fmac_f32_e32 v83, v75, v39
	v_fmac_f32_e32 v84, v75, v43
	v_fmac_f32_e32 v85, v75, v47
	v_add_f32_e32 v37, v49, v137
	v_add_f32_e32 v41, v49, v41
	v_add_f32_e32 v49, v49, v88
	v_fmac_f32_e32 v82, v76, v36
	v_fmac_f32_e32 v83, v76, v40
	v_fmac_f32_e32 v84, v76, v44
	v_fmac_f32_e32 v85, v76, v48
	v_fmac_f32_e32 v82, v77, v37
	v_fmac_f32_e32 v83, v77, v41
	v_fmac_f32_e32 v84, v77, v45
	v_fmac_f32_e32 v85, v77, v49
	s_waitcnt vmcnt(0)
	v_fmac_f32_e32 v82, v78, v50
	v_fmac_f32_e32 v83, v78, v54
	v_fmac_f32_e32 v84, v78, v58
	v_fmac_f32_e32 v85, v78, v62
	v_mul_u32_u24_e32 v87, 10, v225
	v_lshlrev_b32_e32 v1, 9, v1
	v_fmac_f32_e32 v82, v79, v51
	v_fmac_f32_e32 v83, v79, v55
	v_fmac_f32_e32 v84, v79, v59
	v_fmac_f32_e32 v85, v79, v63
	v_lshlrev_b32_e32 v86, 9, v87
	v_lshl_or_b32 v1, v87, 12, v1
	v_lshlrev_b32_e32 v87, 10, v224
	v_fmac_f32_e32 v82, v80, v52
	v_fmac_f32_e32 v83, v80, v56
	v_fmac_f32_e32 v84, v80, v60
	v_fmac_f32_e32 v85, v80, v64
	v_or3_b32 v1, v87, v1, v211
	v_fmac_f32_e32 v82, v81, v53
	v_fmac_f32_e32 v83, v81, v57
	v_fmac_f32_e32 v84, v81, v61
	v_fmac_f32_e32 v85, v81, v65
	v_or3_b32 v86, v86, v212, v214
	v_add_u32_e32 v1, 0x2800, v1
	s_mov_b32 s0, 0
	v_mul_f32_e32 v66, 0.5, v66
	v_mul_f32_e32 v67, 0.5, v67
	v_mul_f32_e32 v68, 0.5, v68
	v_mul_f32_e32 v69, 0.5, v69
	v_mul_f32_e32 v70, 0.5, v70
	v_mul_f32_e32 v71, 0.5, v71
	v_mul_f32_e32 v72, 0.5, v72
	v_mul_f32_e32 v73, 0.5, v73
	v_mul_f32_e32 v74, 0.5, v74
	v_mul_f32_e32 v75, 0.5, v75
	v_mul_f32_e32 v76, 0.5, v76
	v_mul_f32_e32 v77, 0.5, v77
	v_mul_f32_e32 v78, 0.5, v78
	v_mul_f32_e32 v79, 0.5, v79
	v_mul_f32_e32 v80, 0.5, v80
	v_mul_f32_e32 v81, 0.5, v81
	v_mul_f32_e32 v82, 0.5, v82
	v_mul_f32_e32 v83, 0.5, v83
	v_mul_f32_e32 v84, 0.5, v84
	v_mul_f32_e32 v85, 0.5, v85
	v_add_u32_e32 v152, s0, v86
	ds_read_b128 v[88:91], v152
	ds_read_b128 v[92:95], v152 offset:32
	ds_read_b128 v[96:99], v152 offset:64
	ds_read_b128 v[100:103], v152 offset:96
	s_addk_i32 s0, 0x200
.Ltopic_loop:
	v_add_u32_e32 v152, s0, v86
	ds_read_b128 v[136:139], v152
	ds_read_b128 v[140:143], v152 offset:32
	ds_read_b128 v[144:147], v152 offset:64
	ds_read_b128 v[148:151], v152 offset:96
	s_addk_i32 s0, 0x200
	s_waitcnt lgkmcnt(4)
	v_add_f32_e32 v104, v2, v88
	v_add_f32_e32 v108, v6, v88
	v_add_f32_e32 v112, v10, v88
	v_add_f32_e32 v116, v14, v88
	v_add_f32_e32 v105, v3, v89
	v_add_f32_e32 v109, v7, v89
	v_add_f32_e32 v113, v11, v89
	v_add_f32_e32 v117, v15, v89
	v_add_f32_e32 v106, v4, v90
	v_add_f32_e32 v110, v8, v90
	v_add_f32_e32 v114, v12, v90
	v_add_f32_e32 v118, v16, v90
	v_add_f32_e32 v107, v5, v91
	v_add_f32_e32 v111, v9, v91
	v_add_f32_e32 v115, v13, v91
	v_add_f32_e32 v119, v17, v91
	v_mul_f32_e32 v87, v66, v88
	v_fma_f32 v160, v66, |v104|, v82
	v_fma_f32 v161, v66, |v108|, v83
	v_fma_f32 v162, v66, |v112|, v84
	v_fma_f32 v163, v66, |v116|, v85
	v_fmac_f32_e32 v87, v67, v89
	v_fma_f32 v160, v67, |v105|, v160
	v_fma_f32 v161, v67, |v109|, v161
	v_fma_f32 v162, v67, |v113|, v162
	v_fma_f32 v163, v67, |v117|, v163
	v_fmac_f32_e32 v87, v68, v90
	v_fma_f32 v160, v68, |v106|, v160
	v_fma_f32 v161, v68, |v110|, v161
	v_fma_f32 v162, v68, |v114|, v162
	v_fma_f32 v163, v68, |v118|, v163
	v_fmac_f32_e32 v87, v69, v91
	v_fma_f32 v160, v69, |v107|, v160
	v_fma_f32 v161, v69, |v111|, v161
	v_fma_f32 v162, v69, |v115|, v162
	v_fma_f32 v163, v69, |v119|, v163
	v_add_f32_e32 v120, v18, v92
	v_add_f32_e32 v124, v22, v92
	v_add_f32_e32 v128, v26, v92
	v_add_f32_e32 v132, v30, v92
	v_add_f32_e32 v121, v19, v93
	v_add_f32_e32 v125, v23, v93
	v_add_f32_e32 v129, v27, v93
	v_add_f32_e32 v133, v31, v93
	v_add_f32_e32 v122, v20, v94
	v_add_f32_e32 v126, v24, v94
	v_add_f32_e32 v130, v28, v94
	v_add_f32_e32 v134, v32, v94
	v_add_f32_e32 v123, v21, v95
	v_add_f32_e32 v127, v25, v95
	v_add_f32_e32 v131, v29, v95
	v_add_f32_e32 v135, v33, v95
	v_fmac_f32_e32 v87, v70, v92
	v_fma_f32 v160, v70, |v120|, v160
	v_fma_f32 v161, v70, |v124|, v161
	v_fma_f32 v162, v70, |v128|, v162
	v_fma_f32 v163, v70, |v132|, v163
	v_fmac_f32_e32 v87, v71, v93
	v_fma_f32 v160, v71, |v121|, v160
	v_fma_f32 v161, v71, |v125|, v161
	v_fma_f32 v162, v71, |v129|, v162
	v_fma_f32 v163, v71, |v133|, v163
	v_fmac_f32_e32 v87, v72, v94
	v_fma_f32 v160, v72, |v122|, v160
	v_fma_f32 v161, v72, |v126|, v161
	v_fma_f32 v162, v72, |v130|, v162
	v_fma_f32 v163, v72, |v134|, v163
	v_fmac_f32_e32 v87, v73, v95
	v_fma_f32 v160, v73, |v123|, v160
	v_fma_f32 v161, v73, |v127|, v161
	v_fma_f32 v162, v73, |v131|, v162
	v_fma_f32 v163, v73, |v135|, v163
	v_add_f32_e32 v104, v34, v96
	v_add_f32_e32 v108, v38, v96
	v_add_f32_e32 v112, v42, v96
	v_add_f32_e32 v116, v46, v96
	v_add_f32_e32 v105, v35, v97
	v_add_f32_e32 v109, v39, v97
	v_add_f32_e32 v113, v43, v97
	v_add_f32_e32 v117, v47, v97
	v_add_f32_e32 v106, v36, v98
	v_add_f32_e32 v110, v40, v98
	v_add_f32_e32 v114, v44, v98
	v_add_f32_e32 v118, v48, v98
	v_add_f32_e32 v107, v37, v99
	v_add_f32_e32 v111, v41, v99
	v_add_f32_e32 v115, v45, v99
	v_add_f32_e32 v119, v49, v99
	v_fmac_f32_e32 v87, v74, v96
	v_fma_f32 v160, v74, |v104|, v160
	v_fma_f32 v161, v74, |v108|, v161
	v_fma_f32 v162, v74, |v112|, v162
	v_fma_f32 v163, v74, |v116|, v163
	v_fmac_f32_e32 v87, v75, v97
	v_fma_f32 v160, v75, |v105|, v160
	v_fma_f32 v161, v75, |v109|, v161
	v_fma_f32 v162, v75, |v113|, v162
	v_fma_f32 v163, v75, |v117|, v163
	v_fmac_f32_e32 v87, v76, v98
	v_fma_f32 v160, v76, |v106|, v160
	v_fma_f32 v161, v76, |v110|, v161
	v_fma_f32 v162, v76, |v114|, v162
	v_fma_f32 v163, v76, |v118|, v163
	v_fmac_f32_e32 v87, v77, v99
	v_fma_f32 v160, v77, |v107|, v160
	v_fma_f32 v161, v77, |v111|, v161
	v_fma_f32 v162, v77, |v115|, v162
	v_fma_f32 v163, v77, |v119|, v163
	v_add_f32_e32 v120, v50, v100
	v_add_f32_e32 v124, v54, v100
	v_add_f32_e32 v128, v58, v100
	v_add_f32_e32 v132, v62, v100
	v_add_f32_e32 v121, v51, v101
	v_add_f32_e32 v125, v55, v101
	v_add_f32_e32 v129, v59, v101
	v_add_f32_e32 v133, v63, v101
	v_add_f32_e32 v122, v52, v102
	v_add_f32_e32 v126, v56, v102
	v_add_f32_e32 v130, v60, v102
	v_add_f32_e32 v134, v64, v102
	v_add_f32_e32 v123, v53, v103
	v_add_f32_e32 v127, v57, v103
	v_add_f32_e32 v131, v61, v103
	v_add_f32_e32 v135, v65, v103
	v_fmac_f32_e32 v87, v78, v100
	v_fma_f32 v160, v78, |v120|, v160
	v_fma_f32 v161, v78, |v124|, v161
	v_fma_f32 v162, v78, |v128|, v162
	v_fma_f32 v163, v78, |v132|, v163
	v_fmac_f32_e32 v87, v79, v101
	v_fma_f32 v160, v79, |v121|, v160
	v_fma_f32 v161, v79, |v125|, v161
	v_fma_f32 v162, v79, |v129|, v162
	v_fma_f32 v163, v79, |v133|, v163
	v_fmac_f32_e32 v87, v80, v102
	v_fma_f32 v160, v80, |v122|, v160
	v_fma_f32 v161, v80, |v126|, v161
	v_fma_f32 v162, v80, |v130|, v162
	v_fma_f32 v163, v80, |v134|, v163
	v_fmac_f32_e32 v87, v81, v103
	v_fma_f32 v160, v81, |v123|, v160
	v_fma_f32 v161, v81, |v127|, v161
	v_fma_f32 v162, v81, |v131|, v162
	v_fma_f32 v163, v81, |v135|, v163
	v_add_f32_e32 v160, v160, v87
	v_add_f32_e32 v161, v161, v87
	v_add_f32_e32 v162, v162, v87
	v_add_f32_e32 v163, v163, v87
	ds_write2_b32 v1, v160, v161 offset1:32
	ds_write2_b32 v1, v162, v163 offset0:64 offset1:96
	v_add_u32_e32 v1, 0x1000, v1
	v_add_u32_e32 v152, s0, v86
	ds_read_b128 v[88:91], v152
	ds_read_b128 v[92:95], v152 offset:32
	ds_read_b128 v[96:99], v152 offset:64
	ds_read_b128 v[100:103], v152 offset:96
	s_addk_i32 s0, 0x200
	s_waitcnt lgkmcnt(4)
	v_add_f32_e32 v104, v2, v136
	v_add_f32_e32 v108, v6, v136
	v_add_f32_e32 v112, v10, v136
	v_add_f32_e32 v116, v14, v136
	v_add_f32_e32 v105, v3, v137
	v_add_f32_e32 v109, v7, v137
	v_add_f32_e32 v113, v11, v137
	v_add_f32_e32 v117, v15, v137
	v_add_f32_e32 v106, v4, v138
	v_add_f32_e32 v110, v8, v138
	v_add_f32_e32 v114, v12, v138
	v_add_f32_e32 v118, v16, v138
	v_add_f32_e32 v107, v5, v139
	v_add_f32_e32 v111, v9, v139
	v_add_f32_e32 v115, v13, v139
	v_add_f32_e32 v119, v17, v139
	v_mul_f32_e32 v87, v66, v136
	v_fma_f32 v160, v66, |v104|, v82
	v_fma_f32 v161, v66, |v108|, v83
	v_fma_f32 v162, v66, |v112|, v84
	v_fma_f32 v163, v66, |v116|, v85
	v_fmac_f32_e32 v87, v67, v137
	v_fma_f32 v160, v67, |v105|, v160
	v_fma_f32 v161, v67, |v109|, v161
	v_fma_f32 v162, v67, |v113|, v162
	v_fma_f32 v163, v67, |v117|, v163
	v_fmac_f32_e32 v87, v68, v138
	v_fma_f32 v160, v68, |v106|, v160
	v_fma_f32 v161, v68, |v110|, v161
	v_fma_f32 v162, v68, |v114|, v162
	v_fma_f32 v163, v68, |v118|, v163
	v_fmac_f32_e32 v87, v69, v139
	v_fma_f32 v160, v69, |v107|, v160
	v_fma_f32 v161, v69, |v111|, v161
	v_fma_f32 v162, v69, |v115|, v162
	v_fma_f32 v163, v69, |v119|, v163
	v_add_f32_e32 v120, v18, v140
	v_add_f32_e32 v124, v22, v140
	v_add_f32_e32 v128, v26, v140
	v_add_f32_e32 v132, v30, v140
	v_add_f32_e32 v121, v19, v141
	v_add_f32_e32 v125, v23, v141
	v_add_f32_e32 v129, v27, v141
	v_add_f32_e32 v133, v31, v141
	v_add_f32_e32 v122, v20, v142
	v_add_f32_e32 v126, v24, v142
	v_add_f32_e32 v130, v28, v142
	v_add_f32_e32 v134, v32, v142
	v_add_f32_e32 v123, v21, v143
	v_add_f32_e32 v127, v25, v143
	v_add_f32_e32 v131, v29, v143
	v_add_f32_e32 v135, v33, v143
	v_fmac_f32_e32 v87, v70, v140
	v_fma_f32 v160, v70, |v120|, v160
	v_fma_f32 v161, v70, |v124|, v161
	v_fma_f32 v162, v70, |v128|, v162
	v_fma_f32 v163, v70, |v132|, v163
	v_fmac_f32_e32 v87, v71, v141
	v_fma_f32 v160, v71, |v121|, v160
	v_fma_f32 v161, v71, |v125|, v161
	v_fma_f32 v162, v71, |v129|, v162
	v_fma_f32 v163, v71, |v133|, v163
	v_fmac_f32_e32 v87, v72, v142
	v_fma_f32 v160, v72, |v122|, v160
	v_fma_f32 v161, v72, |v126|, v161
	v_fma_f32 v162, v72, |v130|, v162
	v_fma_f32 v163, v72, |v134|, v163
	v_fmac_f32_e32 v87, v73, v143
	v_fma_f32 v160, v73, |v123|, v160
	v_fma_f32 v161, v73, |v127|, v161
	v_fma_f32 v162, v73, |v131|, v162
	v_fma_f32 v163, v73, |v135|, v163
	v_add_f32_e32 v104, v34, v144
	v_add_f32_e32 v108, v38, v144
	v_add_f32_e32 v112, v42, v144
	v_add_f32_e32 v116, v46, v144
	v_add_f32_e32 v105, v35, v145
	v_add_f32_e32 v109, v39, v145
	v_add_f32_e32 v113, v43, v145
	v_add_f32_e32 v117, v47, v145
	v_add_f32_e32 v106, v36, v146
	v_add_f32_e32 v110, v40, v146
	v_add_f32_e32 v114, v44, v146
	v_add_f32_e32 v118, v48, v146
	v_add_f32_e32 v107, v37, v147
	v_add_f32_e32 v111, v41, v147
	v_add_f32_e32 v115, v45, v147
	v_add_f32_e32 v119, v49, v147
	v_fmac_f32_e32 v87, v74, v144
	v_fma_f32 v160, v74, |v104|, v160
	v_fma_f32 v161, v74, |v108|, v161
	v_fma_f32 v162, v74, |v112|, v162
	v_fma_f32 v163, v74, |v116|, v163
	v_fmac_f32_e32 v87, v75, v145
	v_fma_f32 v160, v75, |v105|, v160
	v_fma_f32 v161, v75, |v109|, v161
	v_fma_f32 v162, v75, |v113|, v162
	v_fma_f32 v163, v75, |v117|, v163
	v_fmac_f32_e32 v87, v76, v146
	v_fma_f32 v160, v76, |v106|, v160
	v_fma_f32 v161, v76, |v110|, v161
	v_fma_f32 v162, v76, |v114|, v162
	v_fma_f32 v163, v76, |v118|, v163
	v_fmac_f32_e32 v87, v77, v147
	v_fma_f32 v160, v77, |v107|, v160
	v_fma_f32 v161, v77, |v111|, v161
	v_fma_f32 v162, v77, |v115|, v162
	v_fma_f32 v163, v77, |v119|, v163
	v_add_f32_e32 v120, v50, v148
	v_add_f32_e32 v124, v54, v148
	v_add_f32_e32 v128, v58, v148
	v_add_f32_e32 v132, v62, v148
	v_add_f32_e32 v121, v51, v149
	v_add_f32_e32 v125, v55, v149
	v_add_f32_e32 v129, v59, v149
	v_add_f32_e32 v133, v63, v149
	v_add_f32_e32 v122, v52, v150
	v_add_f32_e32 v126, v56, v150
	v_add_f32_e32 v130, v60, v150
	v_add_f32_e32 v134, v64, v150
	v_add_f32_e32 v123, v53, v151
	v_add_f32_e32 v127, v57, v151
	v_add_f32_e32 v131, v61, v151
	v_add_f32_e32 v135, v65, v151
	v_fmac_f32_e32 v87, v78, v148
	v_fma_f32 v160, v78, |v120|, v160
	v_fma_f32 v161, v78, |v124|, v161
	v_fma_f32 v162, v78, |v128|, v162
	v_fma_f32 v163, v78, |v132|, v163
	v_fmac_f32_e32 v87, v79, v149
	v_fma_f32 v160, v79, |v121|, v160
	v_fma_f32 v161, v79, |v125|, v161
	v_fma_f32 v162, v79, |v129|, v162
	v_fma_f32 v163, v79, |v133|, v163
	v_fmac_f32_e32 v87, v80, v150
	v_fma_f32 v160, v80, |v122|, v160
	v_fma_f32 v161, v80, |v126|, v161
	v_fma_f32 v162, v80, |v130|, v162
	v_fma_f32 v163, v80, |v134|, v163
	v_fmac_f32_e32 v87, v81, v151
	v_fma_f32 v160, v81, |v123|, v160
	v_fma_f32 v161, v81, |v127|, v161
	v_fma_f32 v162, v81, |v131|, v162
	v_fma_f32 v163, v81, |v135|, v163
	v_add_f32_e32 v160, v160, v87
	v_add_f32_e32 v161, v161, v87
	v_add_f32_e32 v162, v162, v87
	v_add_f32_e32 v163, v163, v87
	ds_write2_b32 v1, v160, v161 offset1:32
	ds_write2_b32 v1, v162, v163 offset0:64 offset1:96
	v_add_u32_e32 v1, 0x1000, v1
	s_cmpk_eq_i32 s0, 0x1600
	s_cbranch_scc0 .Ltopic_loop
	v_lshl_or_b32 v1, v227, 12, v226
	s_waitcnt lgkmcnt(0)
	s_barrier
	ds_read2st64_b32 v[2:3], v1 offset0:40 offset1:42
	ds_read2st64_b32 v[4:5], v1 offset0:44 offset1:46
	ds_read2st64_b32 v[6:7], v1 offset0:48 offset1:50
	v_or_b32_e32 v13, 16, v227
	s_waitcnt lgkmcnt(2)
	v_add_f32_e32 v2, s18, v2
	v_add_f32_e32 v8, v2, v3
	ds_read2st64_b32 v[2:3], v1 offset0:52 offset1:54
	s_waitcnt lgkmcnt(2)
	v_add_f32_e32 v4, v8, v4
	v_add_f32_e32 v4, v4, v5
	s_waitcnt lgkmcnt(1)
	v_add_f32_e32 v4, v4, v6
	v_add_f32_e32 v4, v4, v7
	s_waitcnt lgkmcnt(0)
	v_add_f32_e32 v2, v4, v2
	v_add_f32_e32 v2, v2, v3
	v_mul_f32_e32 v2, 0xbfb8aa3b, v2
	v_exp_f32_e32 v2, v2
	s_nop 0
	v_add_f32_e32 v4, 1.0, v2
	v_div_scale_f32 v5, s[0:1], v4, v4, 1.0
	v_rcp_f32_e32 v6, v5
	v_div_scale_f32 v7, vcc, 1.0, v4, 1.0
	ds_read2st64_b32 v[2:3], v1 offset0:104 offset1:106
	v_fma_f32 v8, -v5, v6, 1.0
	v_fmac_f32_e32 v6, v8, v6
	v_mul_f32_e32 v8, v7, v6
	v_fma_f32 v9, -v5, v8, v7
	v_fmac_f32_e32 v8, v9, v6
	v_fma_f32 v5, -v5, v8, v7
	v_div_fmas_f32 v5, v5, v6, v8
	v_div_fixup_f32 v8, v5, v4, 1.0
	ds_read2st64_b32 v[4:5], v1 offset0:108 offset1:110
	ds_read2st64_b32 v[6:7], v1 offset0:112 offset1:114
	s_waitcnt lgkmcnt(2)
	v_add_f32_e32 v2, s18, v2
	v_add_f32_e32 v9, v2, v3
	ds_read2st64_b32 v[2:3], v1 offset0:116 offset1:118
	s_waitcnt lgkmcnt(2)
	v_add_f32_e32 v4, v9, v4
	v_add_f32_e32 v4, v4, v5
	s_waitcnt lgkmcnt(1)
	v_add_f32_e32 v4, v4, v6
	v_add_f32_e32 v4, v4, v7
	s_waitcnt lgkmcnt(0)
	v_add_f32_e32 v2, v4, v2
	v_add_f32_e32 v2, v2, v3
	v_mul_f32_e32 v2, 0xbfb8aa3b, v2
	v_exp_f32_e32 v2, v2
	v_lshlrev_b32_e32 v3, 2, v227
	v_or_b32_e32 v6, 8, v227
	v_mov_b32_e32 v7, 0x17000
	v_add_f32_e32 v10, 1.0, v2
	v_div_scale_f32 v5, s[0:1], v10, v10, 1.0
	v_rcp_f32_e32 v11, v5
	v_or_b32_e32 v4, 0x17000, v3
	v_lshl_or_b32 v12, v6, 2, v7
	v_or_b32_e32 v2, 0x17010, v3
	v_or_b32_e32 v3, 0x17030, v3
	v_lshl_or_b32 v7, v13, 2, v7
	ds_read_b32 v4, v4
	ds_read_b32 v14, v2
	ds_read_b32 v12, v12
	ds_read_b32 v15, v3
	ds_read_b32 v16, v7
	s_waitcnt lgkmcnt(4)
	v_fmaak_f32 v2, v8, v4, 0xbc23d70a
	v_max_f32_e32 v8, 0, v2
	v_fma_f32 v2, -v5, v11, 1.0
	v_fmac_f32_e32 v11, v2, v11
	v_div_scale_f32 v4, vcc, 1.0, v10, 1.0
	v_mul_f32_e32 v17, v4, v11
	v_lshl_or_b32 v18, v6, 12, v226
	ds_read2st64_b32 v[2:3], v18 offset0:40 offset1:42
	v_fma_f32 v6, -v5, v17, v4
	v_fmac_f32_e32 v17, v6, v11
	v_fma_f32 v19, -v5, v17, v4
	ds_read2st64_b32 v[4:5], v18 offset0:44 offset1:46
	ds_read2st64_b32 v[6:7], v18 offset0:48 offset1:50
	s_waitcnt lgkmcnt(2)
	v_add_f32_e32 v2, s18, v2
	v_add_f32_e32 v20, v2, v3
	ds_read2st64_b32 v[2:3], v18 offset0:52 offset1:54
	s_waitcnt lgkmcnt(2)
	v_add_f32_e32 v4, v20, v4
	v_add_f32_e32 v4, v4, v5
	s_waitcnt lgkmcnt(1)
	v_add_f32_e32 v4, v4, v6
	v_add_f32_e32 v4, v4, v7
	s_waitcnt lgkmcnt(0)
	v_add_f32_e32 v2, v4, v2
	v_add_f32_e32 v2, v2, v3
	v_mul_f32_e32 v2, 0xbfb8aa3b, v2
	v_exp_f32_e32 v2, v2
	v_div_fmas_f32 v3, v19, v11, v17
	v_div_fixup_f32 v3, v3, v10, 1.0
	v_mov_b32_e32 v9, 0xbc23d70a
	v_add_f32_e32 v10, 1.0, v2
	v_div_scale_f32 v4, s[0:1], v10, v10, 1.0
	v_rcp_f32_e32 v11, v4
	v_fmaak_f32 v2, v3, v14, 0xbc23d70a
	v_max_f32_e32 v2, 0, v2
	v_add_f32_e32 v8, v8, v2
	v_fma_f32 v2, -v4, v11, 1.0
	v_fmac_f32_e32 v11, v2, v11
	v_div_scale_f32 v5, vcc, 1.0, v10, 1.0
	v_mul_f32_e32 v14, v5, v11
	ds_read2st64_b32 v[2:3], v1 offset0:232 offset1:234
	v_fma_f32 v6, -v4, v14, v5
	v_fmac_f32_e32 v14, v6, v11
	v_fma_f32 v17, -v4, v14, v5
	ds_read2st64_b32 v[4:5], v1 offset0:236 offset1:238
	ds_read2st64_b32 v[6:7], v1 offset0:240 offset1:242
	s_waitcnt lgkmcnt(2)
	v_add_f32_e32 v2, s18, v2
	v_add_f32_e32 v18, v2, v3
	ds_read2st64_b32 v[2:3], v1 offset0:244 offset1:246
	s_waitcnt lgkmcnt(2)
	v_add_f32_e32 v1, v18, v4
	v_add_f32_e32 v1, v1, v5
	s_waitcnt lgkmcnt(1)
	v_add_f32_e32 v1, v1, v6
	v_add_f32_e32 v1, v1, v7
	s_waitcnt lgkmcnt(0)
	v_add_f32_e32 v1, v1, v2
	v_add_f32_e32 v1, v1, v3
	v_mul_f32_e32 v1, 0xbfb8aa3b, v1
	v_exp_f32_e32 v1, v1
	v_div_fmas_f32 v2, v17, v11, v14
	v_div_fixup_f32 v2, v2, v10, 1.0
	v_fmaak_f32 v2, v2, v12, 0xbc23d70a
	v_add_f32_e32 v1, 1.0, v1
	v_div_scale_f32 v4, s[0:1], v1, v1, 1.0
	v_rcp_f32_e32 v10, v4
	v_max_f32_e32 v2, 0, v2
	v_add_f32_e32 v8, v8, v2
	v_div_scale_f32 v5, vcc, 1.0, v1, 1.0
	v_fma_f32 v2, -v4, v10, 1.0
	v_fmac_f32_e32 v10, v2, v10
	v_mul_f32_e32 v11, v5, v10
	v_lshl_or_b32 v12, v13, 12, v226
	ds_read2st64_b32 v[2:3], v12 offset0:40 offset1:42
	v_fma_f32 v6, -v4, v11, v5
	v_fmac_f32_e32 v11, v6, v10
	v_fma_f32 v13, -v4, v11, v5
	ds_read2st64_b32 v[4:5], v12 offset0:44 offset1:46
	ds_read2st64_b32 v[6:7], v12 offset0:48 offset1:50
	s_waitcnt lgkmcnt(2)
	v_add_f32_e32 v2, s18, v2
	v_add_f32_e32 v14, v2, v3
	ds_read2st64_b32 v[2:3], v12 offset0:52 offset1:54
	s_waitcnt lgkmcnt(2)
	v_add_f32_e32 v4, v14, v4
	v_add_f32_e32 v4, v4, v5
	s_waitcnt lgkmcnt(1)
	v_add_f32_e32 v4, v4, v6
	v_add_f32_e32 v4, v4, v7
	s_waitcnt lgkmcnt(0)
	v_add_f32_e32 v2, v4, v2
	v_add_f32_e32 v2, v2, v3
	v_mul_f32_e32 v2, 0xbfb8aa3b, v2
	v_exp_f32_e32 v2, v2
	v_div_fmas_f32 v3, v13, v10, v11
	v_div_fixup_f32 v1, v3, v1, 1.0
	v_fmaak_f32 v1, v1, v15, 0xbc23d70a
	v_add_f32_e32 v2, 1.0, v2
	v_div_scale_f32 v3, s[0:1], v2, v2, 1.0
	v_rcp_f32_e32 v4, v3
	v_max_f32_e32 v1, 0, v1
	v_add_f32_e32 v1, v8, v1
	s_lshl_b32 s0, s42, 5
	v_fma_f32 v5, -v3, v4, 1.0
	v_fmac_f32_e32 v4, v5, v4
	v_div_scale_f32 v5, vcc, 1.0, v2, 1.0
	v_mul_f32_e32 v6, v5, v4
	v_fma_f32 v7, -v3, v6, v5
	v_fmac_f32_e32 v6, v7, v4
	v_fma_f32 v3, -v3, v6, v5
	v_div_fmas_f32 v3, v3, v4, v6
	v_div_fixup_f32 v2, v3, v2, 1.0
	v_fmac_f32_e32 v9, v2, v16
	v_max_f32_e32 v2, 0, v9
	v_add_f32_e32 v2, v1, v2
	v_mov_b32_e32 v1, 0x16800
	v_lshl_or_b32 v1, v0, 2, v1
	v_cmp_gt_u32_e32 vcc, s0, v0
	ds_write_b32 v1, v2
	s_waitcnt lgkmcnt(0)
	s_barrier
	s_and_saveexec_b64 s[0:1], vcc
	s_cbranch_execz .LBB1_57
	ds_read2st64_b32 v[2:3], v1 offset1:2
	ds_read2st64_b32 v[4:5], v1 offset0:4 offset1:6
	v_add_u32_e32 v0, s33, v0
	v_ashrrev_i32_e32 v1, 31, v0
	v_lshl_add_u64 v[6:7], v[0:1], 2, s[10:11]
	s_waitcnt lgkmcnt(1)
	v_add_f32_e32 v1, v2, v3
	s_waitcnt lgkmcnt(0)
	v_add_f32_e32 v1, v1, v4
	v_add_f32_e32 v1, v1, v5
	v_add_u32_e32 v0, 0x7d00, v0
	v_mul_f32_e32 v2, 0x3d4ccccd, v1
	v_ashrrev_i32_e32 v1, 31, v0
	v_lshl_add_u64 v[0:1], v[0:1], 2, s[10:11]
	global_store_dword v[6:7], v2, off
	global_store_dword v[0:1], v2, off
